# adds: arrive without waiting for partial-sum store completion (NaN-tagged partials with retry), per-batch arrival counters, faster poll
# speedup vs baseline: 1.0082x; 1.0082x over previous
amdhsa.kernels:
  - .agpr_count:     0
    .args:
      - .actual_access:  read_only
        .address_space:  global
        .offset:         0
        .size:           8
        .value_kind:     global_buffer
      - .actual_access:  read_only
        .address_space:  global
        .offset:         8
        .size:           8
        .value_kind:     global_buffer
      - .actual_access:  read_only
        .address_space:  global
        .offset:         16
        .size:           8
        .value_kind:     global_buffer
      - .actual_access:  read_only
        .address_space:  global
        .offset:         24
        .size:           8
        .value_kind:     global_buffer
      - .actual_access:  read_only
        .address_space:  global
        .offset:         32
        .size:           8
        .value_kind:     global_buffer
      - .actual_access:  read_only
        .address_space:  global
        .offset:         40
        .size:           8
        .value_kind:     global_buffer
      - .actual_access:  read_only
        .address_space:  global
        .offset:         48
        .size:           8
        .value_kind:     global_buffer
      - .actual_access:  read_only
        .address_space:  global
        .offset:         56
        .size:           8
        .value_kind:     global_buffer
      - .actual_access:  write_only
        .address_space:  global
        .offset:         64
        .size:           8
        .value_kind:     global_buffer
      - .actual_access:  write_only
        .address_space:  global
        .offset:         72
        .size:           8
        .value_kind:     global_buffer
      - .actual_access:  write_only
        .address_space:  global
        .offset:         80
        .size:           8
        .value_kind:     global_buffer
      - .actual_access:  write_only
        .address_space:  global
        .offset:         88
        .size:           8
        .value_kind:     global_buffer
    .group_segment_fixed_size: 512
    .kernarg_segment_align: 8
    .kernarg_segment_size: 96
    .language:       OpenCL C
    .language_version:
      - 2
      - 0
    .max_flat_workgroup_size: 256
    .name:           _Z11prep_kernelPKfS0_S0_S0_S0_S0_S0_S0_PDF16_PfS2_Pj
    .private_segment_fixed_size: 0
    .sgpr_count:     18
    .sgpr_spill_count: 0
    .symbol:         _Z11prep_kernelPKfS0_S0_S0_S0_S0_S0_S0_PDF16_PfS2_Pj.kd
    .uniform_work_group_size: 1
    .uses_dynamic_stack: false
    .vgpr_count:     67
    .vgpr_spill_count: 0
    .wavefront_size: 64
  - .agpr_count:     0
    .args:
      - .actual_access:  read_only
        .address_space:  global
        .offset:         0
        .size:           8
        .value_kind:     global_buffer
      - .actual_access:  read_only
        .address_space:  global
        .offset:         8
        .size:           8
        .value_kind:     global_buffer
      - .actual_access:  read_only
        .address_space:  global
        .offset:         16
        .size:           8
        .value_kind:     global_buffer
      - .address_space:  global
        .offset:         24
        .size:           8
        .value_kind:     global_buffer
      - .address_space:  global
        .offset:         32
        .size:           8
        .value_kind:     global_buffer
      - .actual_access:  read_only
        .address_space:  global
        .offset:         40
        .size:           8
        .value_kind:     global_buffer
      - .actual_access:  read_only
        .address_space:  global
        .offset:         48
        .size:           8
        .value_kind:     global_buffer
      - .actual_access:  read_only
        .address_space:  global
        .offset:         56
        .size:           8
        .value_kind:     global_buffer
      - .actual_access:  read_only
        .address_space:  global
        .offset:         64
        .size:           8
        .value_kind:     global_buffer
      - .actual_access:  read_only
        .address_space:  global
        .offset:         72
        .size:           8
        .value_kind:     global_buffer
      - .actual_access:  read_only
        .address_space:  global
        .offset:         80
        .size:           8
        .value_kind:     global_buffer
      - .actual_access:  read_only
        .address_space:  global
        .offset:         88
        .size:           8
        .value_kind:     global_buffer
      - .actual_access:  read_only
        .address_space:  global
        .offset:         96
        .size:           8
        .value_kind:     global_buffer
      - .actual_access:  read_only
        .address_space:  global
        .offset:         104
        .size:           8
        .value_kind:     global_buffer
      - .actual_access:  read_only
        .address_space:  global
        .offset:         112
        .size:           8
        .value_kind:     global_buffer
      - .actual_access:  read_only
        .address_space:  global
        .offset:         120
        .size:           8
        .value_kind:     global_buffer
      - .actual_access:  write_only
        .address_space:  global
        .offset:         128
        .size:           8
        .value_kind:     global_buffer
    .group_segment_fixed_size: 163840
    .kernarg_segment_align: 8
    .kernarg_segment_size: 136
    .language:       OpenCL C
    .language_version:
      - 2
      - 0
    .max_flat_workgroup_size: 512
    .name:           _Z12fused_kernelPKfPKiPKDF16_PfPjS0_S0_S0_S0_S0_S0_S0_S0_S0_S0_S0_S5_
    .private_segment_fixed_size: 0
    .sgpr_count:     84
    .sgpr_spill_count: 0
    .symbol:         _Z12fused_kernelPKfPKiPKDF16_PfPjS0_S0_S0_S0_S0_S0_S0_S0_S0_S0_S0_S5_.kd
    .uniform_work_group_size: 1
    .uses_dynamic_stack: false
    .vgpr_count:     256
    .vgpr_spill_count: 0
    .wavefront_size: 64
